# dn_prep unit offset by 128 workgroups so its extra unit lands on the workgroups that have one lru_prep unit fewer
# speedup vs baseline: 1.0310x; 1.0051x over previous
.LBB0_437:
	v_readlane_b32 s4, v252, 48
	s_waitcnt lgkmcnt(0)
	s_barrier
	v_readlane_b32 s5, v252, 49
	s_andn2_b64 vcc, exec, s[4:5]
	s_cbranch_vccnz .LBB0_653
	v_readlane_b32 s4, v255, 5
	v_bfe_u32 v2, v108, 7, 2
	s_mul_i32 s68, s4, 0x1800
	s_lshl_b32 s8, s4, 3
	v_mul_u32_u24_e32 v2, 0x600, v2
	s_movk_i32 s2, 0x7f
	s_mov_b32 s4, 0x2aaaaaab
	v_and_or_b32 v64, v108, s2, v2
	v_mul_hi_i32 v2, v108, s4
	s_movk_i32 s2, 0xc90
	v_lshrrev_b32_e32 v3, 31, v2
	v_ashrrev_i32_e32 v2, 3, v2
	v_cmp_gt_i32_e64 s[40:41], s2, v108
	v_mul_hi_i32 v4, v125, s4
	s_movk_i32 s2, 0xa90
	v_add_u32_e32 v68, v2, v3
	v_lshrrev_b32_e32 v5, 31, v4
	v_ashrrev_i32_e32 v4, 3, v4
	v_cmp_gt_i32_e64 s[42:43], s2, v108
	s_movk_i32 s2, 0x890
	v_mul_lo_u32 v2, v68, 48
	v_add_u32_e32 v69, v4, v5
	v_mul_hi_i32 v10, v124, s4
	v_cmp_gt_i32_e64 s[44:45], s2, v108
	s_movk_i32 s2, 0x690
	v_sub_u32_e32 v3, v108, v2
	v_mul_lo_u32 v4, v69, 48
	v_lshrrev_b32_e32 v11, 31, v10
	v_ashrrev_i32_e32 v10, 3, v10
	v_mul_hi_i32 v14, v123, s4
	v_cmp_gt_i32_e64 s[46:47], s2, v108
	s_movk_i32 s2, 0x490
	v_lshlrev_b32_e32 v2, 5, v3
	v_sub_u32_e32 v5, v125, v4
	v_add_u32_e32 v70, v10, v11
	v_lshrrev_b32_e32 v15, 31, v14
	v_ashrrev_i32_e32 v14, 3, v14
	v_mul_hi_i32 v18, v128, s4
	v_cmp_gt_i32_e64 s[48:49], s2, v108
	s_movk_i32 s2, 0x290
	v_and_b32_e32 v6, 0xfffffe00, v2
	v_lshlrev_b32_e32 v2, 3, v3
	v_lshlrev_b32_e32 v4, 5, v5
	v_mul_lo_u32 v10, v70, 48
	v_add_u32_e32 v71, v14, v15
	v_lshrrev_b32_e32 v19, 31, v18
	v_ashrrev_i32_e32 v18, 3, v18
	v_mul_hi_i32 v22, v127, s4
	v_cmp_gt_i32_e64 s[50:51], s2, v108
	s_movk_i32 s2, 0x310
	v_lshlrev_b32_e32 v3, 4, v3
	v_and_b32_e32 v8, 0xfffffe00, v4
	v_lshlrev_b32_e32 v4, 3, v5
	v_sub_u32_e32 v13, v124, v10
	v_mul_lo_u32 v14, v71, 48
	v_add_u32_e32 v72, v18, v19
	v_lshrrev_b32_e32 v23, 31, v22
	v_ashrrev_i32_e32 v22, 3, v22
	v_mul_lo_u32 v30, v68, s2
	v_and_b32_e32 v31, 0xffffff00, v3
	v_lshlrev_b32_e32 v5, 4, v5
	v_lshlrev_b32_e32 v10, 5, v13
	v_lshlrev_b32_e32 v12, 3, v13
	v_sub_u32_e32 v17, v123, v14
	v_mul_lo_u32 v18, v72, 48
	v_add_u32_e32 v73, v22, v23
	v_add3_u32 v30, 0, v30, v31
	v_mul_lo_u32 v31, v69, s2
	v_and_b32_e32 v32, 0xffffff00, v5
	v_lshlrev_b32_e32 v13, 4, v13
	v_lshlrev_b32_e32 v14, 5, v17
	v_lshlrev_b32_e32 v16, 3, v17
	v_sub_u32_e32 v21, v128, v18
	v_mul_lo_u32 v22, v73, 48
	v_add3_u32 v31, 0, v31, v32
	v_mul_lo_u32 v32, v70, s2
	v_and_b32_e32 v33, 0xffffff00, v13
	v_lshlrev_b32_e32 v17, 4, v17
	v_lshlrev_b32_e32 v18, 5, v21
	v_lshlrev_b32_e32 v20, 3, v21
	v_sub_u32_e32 v25, v127, v22
	v_mul_hi_i32 v26, v126, s4
	v_add3_u32 v32, 0, v32, v33
	v_mul_lo_u32 v33, v71, s2
	v_and_b32_e32 v34, 0xffffff00, v17
	v_lshlrev_b32_e32 v21, 4, v21
	s_cmp_lt_u32 s56, 64
	v_lshlrev_b32_e32 v22, 5, v25
	v_lshlrev_b32_e32 v24, 3, v25
	v_lshrrev_b32_e32 v27, 31, v26
	v_ashrrev_i32_e32 v26, 3, v26
	v_add3_u32 v33, 0, v33, v34
	v_mul_lo_u32 v34, v72, s2
	v_and_b32_e32 v35, 0xffffff00, v21
	v_lshlrev_b32_e32 v25, 4, v25
	s_cselect_b64 s[90:91], -1, 0
	s_cmp_gt_u32 s56, 63
	v_add_u32_e32 v74, v26, v27
	v_add3_u32 v49, 0, v34, v35
	v_mul_lo_u32 v34, v73, s2
	v_and_b32_e32 v35, 0xffffff00, v25
	s_cselect_b64 s[92:93], -1, 0
	s_add_i32 s27, 0, 0x1a000
	v_add3_u32 v51, 0, v34, v35
	v_mul_lo_u32 v34, v74, s2
	v_mul_lo_u32 v60, v122, s2
	s_bfe_u32 s2, s56, 0x20006
	s_cmp_gt_u32 s61, 3
	v_readlane_b32 s5, v255, 6
	v_mul_lo_u32 v26, v74, 48
	s_mov_b64 s[58:59], s[94:95]
	s_cselect_b64 s[94:95], -1, 0
	s_cmp_lt_u32 s61, 4
	v_sub_u32_e32 v29, v126, v26
	s_cselect_b32 s4, 0x4400, 0
	s_mov_b32 s5, 0x8800
	s_mov_b32 s6, 0x11000
	s_mul_i32 s10, s61, 3
	v_lshlrev_b32_e32 v26, 5, v29
	v_lshlrev_b32_e32 v28, 3, v29
	v_lshlrev_b32_e32 v29, 4, v29
	s_cselect_b32 s5, s5, 0x4400
	s_cselect_b32 s6, s6, 0x13400
	s_add_i32 s66, s4, 0
	s_lshl_b32 s83, s2, 4
	s_add_i32 s17, s10, 13
	v_and_b32_e32 v35, 0xffffff00, v29
	s_cmp_gt_i32 s61, 2
	s_mul_i32 s4, s61, 0x440
	v_add3_u32 v53, 0, v34, v35
	v_and_b32_e32 v34, 7, v108
	s_mov_b32 s60, s96
	s_cselect_b64 s[96:97], -1, 0
	s_xor_b32 s60, s60, 0x80
	s_add_i32 s4, s4, 0
	v_ashrrev_i32_e32 v35, 7, v108
	v_lshrrev_b32_e32 v36, 4, v109
	v_lshlrev_b32_e32 v55, 5, v34
	v_lshlrev_b32_e32 v57, 6, v34
	v_mul_lo_u32 v34, v122, s14
	s_add_i32 s4, s4, 0x1e400
	s_waitcnt lgkmcnt(0)
	v_cmp_ge_i32_e64 s[54:55], v35, v36
	v_lshlrev_b32_e32 v35, 2, v109
	s_lshl_b32 s2, s2, 6
	v_add_u32_e32 v61, 0, v34
	v_writelane_b32 v255, s4, 8
	v_add3_u32 v76, s27, v34, v35
	v_mul_lo_u32 v34, v122, s25
	s_add_i32 s4, 0, 0x11000
	s_add_i32 s2, s2, 0
	v_add_u32_e32 v62, s4, v34
	s_add_i32 s4, 0, 0x13400
	v_writelane_b32 v255, s2, 9
	s_add_i32 s65, s2, s5
	s_lshl_b32 s2, s61, 13
	v_add_u32_e32 v63, s4, v34
	s_or_b32 s4, s2, 0x1000
	v_writelane_b32 v255, s4, 10
	s_or_b32 s4, s2, 0x400
	v_writelane_b32 v255, s4, 11
	s_or_b32 s4, s2, 0x1400
	v_writelane_b32 v255, s4, 12
	s_or_b32 s4, s2, 0x800
	v_writelane_b32 v255, s4, 13
	s_or_b32 s4, s2, 0x1800
	v_writelane_b32 v255, s4, 14
	s_or_b32 s4, s2, 0xc00
	v_writelane_b32 v255, s4, 15
	s_or_b32 s4, s2, 0x1c00
	s_lshl_b32 s18, s61, 2
	v_writelane_b32 v255, s4, 16
	s_lshl_b32 s12, s61, 5
	s_lshl_b32 s4, s61, 3
	s_add_i32 s18, s18, 25
	s_and_b32 s13, s56, 0xffffffc0
	s_add_i32 s24, s6, 0
	s_lshl_b32 s28, s61, 1
	s_add_i32 s29, s12, 0
	s_lshl_b32 s20, s61, 4
	s_and_b32 s19, s4, -16
	s_cmp_gt_u32 s28, 31
	s_cselect_b64 s[4:5], -1, 0
	s_cmp_gt_u32 s28, 39
	v_readlane_b32 s9, v253, 45
	s_cselect_b64 s[6:7], -1, 0
	s_or_b32 s8, s9, s8
	v_writelane_b32 v255, s8, 17
	s_mul_i32 s8, s61, 0x60
	s_addk_i32 s8, 0x1a0
	v_writelane_b32 v255, s8, 18
	s_mul_i32 s8, s61, 0xc0
	s_addk_i32 s8, 0x340
	v_writelane_b32 v255, s8, 19
	s_mul_i32 s8, s61, 24
	s_addk_i32 s8, 0x68
	v_writelane_b32 v255, s8, 20
	s_mul_i32 s8, s61, 12
	s_add_i32 s8, s8, 52
	s_ashr_i32 s11, s10, 31
	v_writelane_b32 v255, s8, 21
	s_lshl_b64 s[8:9], s[10:11], 10
	v_readlane_b32 s10, v254, 9
	s_add_u32 s8, s10, s8
	v_writelane_b32 v255, s8, 22
	v_readlane_b32 s8, v254, 10
	s_addc_u32 s8, s8, s9
	v_and_b32_e32 v10, 0xfffffe00, v10
	v_writelane_b32 v255, s8, 23
	s_lshl_b32 s8, s61, 7
	s_addk_i32 s8, 0x320
	v_writelane_b32 v255, s8, 24
	s_lshl_b32 s8, s61, 8
	s_addk_i32 s8, 0x640
	v_writelane_b32 v255, s8, 25
	s_add_i32 s8, s12, 0xc8
	v_writelane_b32 v255, s8, 26
	s_add_i32 s8, s20, 0x64
	v_writelane_b32 v255, s8, 27
	s_mul_i32 s8, s61, 0x1140
	s_add_i32 s8, s8, 0xdd00
	v_and_b32_e32 v14, 0xfffffe00, v14
	v_and_b32_e32 v18, 0xfffffe00, v18
	v_and_b32_e32 v22, 0xfffffe00, v22
	v_and_b32_e32 v26, 0xfffffe00, v26
	v_writelane_b32 v255, s8, 28
	s_mul_i32 s8, s61, 0x1100
	v_ashrrev_i32_e32 v7, 31, v6
	v_and_b32_e32 v2, 0x78, v2
	v_ashrrev_i32_e32 v9, 31, v8
	v_and_b32_e32 v4, 0x78, v4
	v_ashrrev_i32_e32 v11, 31, v10
	v_and_b32_e32 v12, 0x78, v12
	v_ashrrev_i32_e32 v15, 31, v14
	v_and_b32_e32 v16, 0x78, v16
	v_ashrrev_i32_e32 v19, 31, v18
	v_and_b32_e32 v20, 0x78, v20
	v_ashrrev_i32_e32 v23, 31, v22
	v_and_b32_e32 v24, 0x78, v24
	v_ashrrev_i32_e32 v27, 31, v26
	v_and_b32_e32 v28, 0x78, v28
	v_and_b32_e32 v3, 0xf0, v3
	v_and_b32_e32 v5, 0xf0, v5
	v_and_b32_e32 v13, 0xf0, v13
	v_and_b32_e32 v17, 0xf0, v17
	v_and_b32_e32 v21, 0xf0, v21
	v_and_b32_e32 v25, 0xf0, v25
	v_and_b32_e32 v29, 0xf0, v29
	v_add_u32_e32 v59, 0, v55
	v_add_u32_e32 v77, s67, v35
	v_writelane_b32 v255, s13, 29
	s_add_i32 s8, s8, s13
	v_and_b32_e32 v65, 0xfffffe00, v108
	v_and_b32_e32 v66, 0xfffffe00, v125
	v_and_b32_e32 v67, 0xfffffe00, v124
	v_cmp_gt_i32_e64 s[52:53], s25, v108
	v_lshl_add_u32 v75, v108, 2, s27
	v_add_u32_e32 v78, 4, v77
	v_add_u32_e32 v79, 8, v77
	v_add_u32_e32 v80, 12, v77
	v_add_u32_e32 v81, 16, v77
	v_add_u32_e32 v82, 20, v77
	v_add_u32_e32 v83, 24, v77
	v_add_u32_e32 v84, 28, v77
	v_lshl_add_u64 v[34:35], v[6:7], 1, s[58:59]
	v_lshl_add_u64 v[36:37], v[8:9], 1, s[58:59]
	v_lshl_add_u64 v[38:39], v[10:11], 1, s[58:59]
	v_lshl_add_u64 v[40:41], v[14:15], 1, s[58:59]
	v_lshl_add_u64 v[42:43], v[18:19], 1, s[58:59]
	v_lshl_add_u64 v[44:45], v[22:23], 1, s[58:59]
	v_lshl_add_u64 v[46:47], v[26:27], 1, s[58:59]
	v_writelane_b32 v255, s8, 30
	s_lshl_b64 s[8:9], s[68:69], 2
	v_lshlrev_b32_e32 v98, 1, v2
	v_lshlrev_b32_e32 v48, 1, v4
	v_lshlrev_b32_e32 v50, 1, v12
	v_lshlrev_b32_e32 v52, 1, v16
	v_lshlrev_b32_e32 v54, 1, v20
	v_lshlrev_b32_e32 v56, 1, v24
	v_lshlrev_b32_e32 v58, 1, v28
	v_add_u32_e32 v85, v30, v3
	v_add_u32_e32 v86, v31, v5
	v_add_u32_e32 v87, v32, v13
	v_add_u32_e32 v88, v33, v17
	v_add_u32_e32 v89, v49, v21
	v_add_u32_e32 v90, v51, v25
	v_add_u32_e32 v91, v53, v29
	v_add_u32_e32 v92, 0, v57
	v_add_u32_e32 v93, v59, v60
	v_add_u32_e32 v94, v61, v55
	v_add_u32_e32 v95, v62, v143
	v_add_u32_e32 v96, v63, v143
	s_branch .LBB0_440
